# baseline (speedup 1.0000x reference)
_Z5k_outPKiPKfPf:
	s_load_dwordx4 s[4:7], s[0:1], 0x0
	s_lshl_b32 s3, s2, 8
	v_add_u32_e32 v0, s3, v0
	s_load_dwordx2 s[2:3], s[0:1], 0x10
	v_cmp_gt_i32_e32 vcc, 0x500, v0
	s_and_saveexec_b64 s[0:1], vcc
	s_cbranch_execz .LBB3_2
	s_mov_b32 s0, 0x66666667
	v_mul_hi_i32 v1, v0, s0
	v_lshrrev_b32_e32 v2, 31, v1
	v_ashrrev_i32_e32 v1, 2, v1
	v_add_u32_e32 v1, v1, v2
	v_mul_lo_u32 v2, v1, 10
	v_mul_lo_u32 v4, v1, 11
	v_sub_u32_e32 v2, v0, v2
	v_ashrrev_i32_e32 v5, 31, v4
	v_add_u32_e32 v12, v4, v2
	s_waitcnt lgkmcnt(0)
	v_lshl_add_u64 v[14:15], v[4:5], 2, s[4:5]
	s_movk_i32 s0, 0x1000
	v_add_u32_e32 v4, 0x580, v12
	v_add_co_u32_e32 v28, vcc, s0, v14
	v_ashrrev_i32_e32 v5, 31, v4
	s_nop 0
	v_addc_co_u32_e32 v29, vcc, 0, v15, vcc
	s_movk_i32 s0, 0x2000
	v_lshl_add_u64 v[26:27], v[4:5], 2, s[4:5]
	v_add_u32_e32 v4, 0xb00, v12
	v_add_co_u32_e32 v32, vcc, s0, v14
	v_ashrrev_i32_e32 v5, 31, v4
	s_nop 0
	v_addc_co_u32_e32 v33, vcc, 0, v15, vcc
	s_movk_i32 s0, 0x4000
	v_ashrrev_i32_e32 v13, 31, v12
	v_lshl_add_u64 v[30:31], v[4:5], 2, s[4:5]
	v_add_u32_e32 v4, 0x1080, v12
	v_add_co_u32_e32 v36, vcc, s0, v14
	v_lshl_add_u64 v[24:25], v[12:13], 2, s[4:5]
	v_ashrrev_i32_e32 v5, 31, v4
	v_addc_co_u32_e32 v37, vcc, 0, v15, vcc
	s_movk_i32 s0, 0x5000
	v_lshl_add_u64 v[34:35], v[4:5], 2, s[4:5]
	global_load_dword v4, v[24:25], off
	global_load_dword v16, v[14:15], off offset:40
	global_load_dword v6, v[26:27], off
	global_load_dword v20, v[28:29], off offset:1576
	global_load_dword v8, v[30:31], off
	global_load_dword v18, v[32:33], off offset:3112
	global_load_dword v10, v[34:35], off
	global_load_dword v22, v[36:37], off offset:552
	v_add_co_u32_e32 v26, vcc, s0, v14
	s_movk_i32 s0, 0x6000
	s_nop 0
	v_addc_co_u32_e32 v27, vcc, 0, v15, vcc
	v_add_co_u32_e32 v30, vcc, s0, v14
	s_mov_b32 s0, 0x8000
	s_nop 0
	v_addc_co_u32_e32 v31, vcc, 0, v15, vcc
	v_add_u32_e32 v24, 0x1600, v12
	v_add_co_u32_e32 v32, vcc, s0, v14
	v_ashrrev_i32_e32 v25, 31, v24
	v_add_u32_e32 v28, 0x1b80, v12
	v_addc_co_u32_e32 v33, vcc, 0, v15, vcc
	s_mov_b32 s0, 0x9000
	v_lshl_add_u64 v[24:25], v[24:25], 2, s[4:5]
	v_ashrrev_i32_e32 v29, 31, v28
	v_add_co_u32_e32 v14, vcc, s0, v14
	v_lshl_add_u64 v[28:29], v[28:29], 2, s[4:5]
	global_load_dword v34, v[24:25], off
	global_load_dword v36, v[26:27], off offset:2088
	global_load_dword v38, v[28:29], off
	global_load_dword v40, v[30:31], off offset:3624
	global_load_dword v42, v[32:33], off offset:1064
	v_addc_co_u32_e32 v15, vcc, 0, v15, vcc
	global_load_dword v14, v[14:15], off offset:2600
	v_add_u32_e32 v24, 0x2100, v12
	v_ashrrev_i32_e32 v25, 31, v24
	v_add_u32_e32 v12, 0x2680, v12
	v_lshl_add_u64 v[24:25], v[24:25], 2, s[4:5]
	v_ashrrev_i32_e32 v13, 31, v12
	v_lshl_add_u64 v[12:13], v[12:13], 2, s[4:5]
	global_load_dword v26, v[24:25], off
	global_load_dword v28, v[12:13], off
	v_ashrrev_i32_e32 v3, 31, v2
	v_lshl_add_u64 v[2:3], v[2:3], 2, s[6:7]
	global_load_dword v1, v[2:3], off
	global_load_dword v12, v[2:3], off offset:40
	global_load_dword v13, v[2:3], off offset:80
	global_load_dword v24, v[2:3], off offset:120
	global_load_dword v25, v[2:3], off offset:160
	s_waitcnt vmcnt(20)
	v_ashrrev_i32_e32 v5, 31, v4
	s_waitcnt vmcnt(19)
	v_ashrrev_i32_e32 v17, 31, v16
	s_waitcnt vmcnt(18)
	v_ashrrev_i32_e32 v7, 31, v6
	s_waitcnt vmcnt(17)
	v_ashrrev_i32_e32 v21, 31, v20
	v_lshl_add_u64 v[2:3], v[16:17], 0, v[20:21]
	s_waitcnt vmcnt(15)
	v_ashrrev_i32_e32 v19, 31, v18
	v_lshl_add_u64 v[2:3], v[2:3], 0, v[18:19]
	s_waitcnt vmcnt(13)
	v_ashrrev_i32_e32 v23, 31, v22
	v_lshl_add_u64 v[2:3], v[2:3], 0, v[22:23]
	v_ashrrev_i32_e32 v9, 31, v8
	v_ashrrev_i32_e32 v11, 31, v10
	s_waitcnt vmcnt(12)
	v_ashrrev_i32_e32 v35, 31, v34
	s_waitcnt vmcnt(11)
	v_ashrrev_i32_e32 v37, 31, v36
	v_lshl_add_u64 v[2:3], v[2:3], 0, v[36:37]
	s_waitcnt vmcnt(9)
	v_ashrrev_i32_e32 v41, 31, v40
	v_lshl_add_u64 v[2:3], v[2:3], 0, v[40:41]
	s_waitcnt vmcnt(8)
	v_ashrrev_i32_e32 v43, 31, v42
	v_lshl_add_u64 v[2:3], v[2:3], 0, v[42:43]
	s_waitcnt vmcnt(7)
	v_ashrrev_i32_e32 v15, 31, v14
	v_lshl_add_u64 v[2:3], v[2:3], 0, v[14:15]
	v_xor_b32_e32 v14, v2, v3
	v_ashrrev_i32_e32 v14, 31, v14
	v_ffbh_i32_e32 v15, v3
	v_add_u32_e32 v14, 32, v14
	v_add_u32_e32 v15, -1, v15
	v_min_u32_e32 v14, v15, v14
	v_lshlrev_b64 v[2:3], v14, v[2:3]
	v_min_u32_e32 v2, 1, v2
	v_or_b32_e32 v2, v3, v2
	v_cvt_f32_i32_e32 v2, v2
	v_sub_u32_e32 v3, 32, v14
	v_ashrrev_i32_e32 v39, 31, v38
	s_waitcnt vmcnt(6)
	v_ashrrev_i32_e32 v27, 31, v26
	v_ldexp_f32 v2, v2, v3
	v_mul_f32_e32 v14, 0x39800000, v2
	v_lshl_add_u64 v[2:3], v[4:5], 0, v[6:7]
	v_lshl_add_u64 v[2:3], v[2:3], 0, v[8:9]
	v_lshl_add_u64 v[2:3], v[2:3], 0, v[10:11]
	v_lshl_add_u64 v[2:3], v[2:3], 0, v[34:35]
	v_lshl_add_u64 v[2:3], v[2:3], 0, v[38:39]
	s_waitcnt vmcnt(5)
	v_ashrrev_i32_e32 v29, 31, v28
	v_lshl_add_u64 v[2:3], v[2:3], 0, v[26:27]
	v_lshl_add_u64 v[2:3], v[2:3], 0, v[28:29]
	v_xor_b32_e32 v4, v2, v3
	v_ashrrev_i32_e32 v4, 31, v4
	v_ffbh_i32_e32 v5, v3
	v_add_u32_e32 v4, 32, v4
	v_add_u32_e32 v5, -1, v5
	v_min_u32_e32 v4, v5, v4
	v_lshlrev_b64 v[2:3], v4, v[2:3]
	v_min_u32_e32 v2, 1, v2
	v_or_b32_e32 v2, v3, v2
	v_cvt_f32_i32_e32 v2, v2
	v_sub_u32_e32 v4, 32, v4
	v_max_f32_e32 v3, 1.0, v14
	s_waitcnt vmcnt(4)
	v_add_f32_e32 v1, 0, v1
	v_ldexp_f32 v2, v2, v4
	v_mul_f32_e32 v2, 0x39800000, v2
	v_div_scale_f32 v4, s[0:1], v3, v3, v2
	v_rcp_f32_e32 v5, v4
	s_waitcnt vmcnt(3)
	v_add_f32_e32 v1, v1, v12
	s_waitcnt vmcnt(2)
	v_add_f32_e32 v1, v1, v13
	s_waitcnt vmcnt(1)
	v_add_f32_e32 v1, v1, v24
	v_fma_f32 v6, -v4, v5, 1.0
	v_fmac_f32_e32 v5, v6, v5
	v_div_scale_f32 v6, vcc, v2, v3, v2
	v_mul_f32_e32 v7, v6, v5
	v_fma_f32 v8, -v4, v7, v6
	v_fmac_f32_e32 v7, v8, v5
	v_fma_f32 v4, -v4, v7, v6
	v_div_fmas_f32 v4, v4, v5, v7
	s_waitcnt vmcnt(0)
	v_add_f32_e32 v1, v1, v25
	v_div_fixup_f32 v2, v4, v3, v2
	v_add_f32_e32 v2, v2, v1
	v_ashrrev_i32_e32 v1, 31, v0
	v_lshl_add_u64 v[0:1], v[0:1], 2, s[2:3]
	global_store_dword v[0:1], v2, off
